# mixer C unit header: K/V row loads requested right behind the Q loads (before the barrier and the bias-table fill), fill temporaries renamed
# baseline (speedup 1.0000x reference)
; #define LAS __attribute__((address_space(3)))
; __device__ __forceinline__ void mixer_c_shared(const bf16* CQ, const bf16* CK, const bf16* CV  , bf16* O, const float* rel_bias, const float* sink, LAS unsigned char* lds, int G, int blk, int tid, int lane, int wave) {
;     ...
;         const int kvh = su & 3, v = su >> 2, b = v >> 5, q0 = 256 * (v & 31), w0 = q0 - 128;
;         const size_t tb0 = (size_t)b * SEQ;
;         const int i5 = lane & 31, hh = lane >> 5, q0w = q0 + 32 * wave, tq = q0w + i5;
;         const bf16* qp = CQ + (tb0 + tq) * 1024 + (4 * kvh) * 64 + 8 * hh;
;         bf16x8 qn[4];
; #pragma unroll
;         for (int d0 = 0; d0 < 4; ++d0) qn[d0] = *(const bf16x8*)(qp + 16 * d0);
;         __syncthreads();
;         for (int idx = tid; idx < TC_LEN; idx += NWAVES * 64) { const int i = idx - TC_OFF; const bool in = (i >= 0 && i <= 256); const int bk = in ? t5_bucket(i - 128) : 0;
; #pragma unroll
;             for (int j = 0; j < 4; ++j) tab4[j * TC_LEN + idx] = in ? (rel_bias[(4 * kvh + j) * 32 + bk] * LOG2E + 64.0f) * KAPPA : -1.0f; }
; #pragma unroll
;         for (int half = 0; half < 2; ++half) {
;             v4u kv[4], vv[4];
; #pragma unroll
;             for (int i = 0; i < 4; ++i) { const int c = tid + 512 * (4 * half + i), rw = c >> 3, ch = c & 7, key = w0 + rw; const bool ok = key >= 0 && key < SEQ; const size_t ro = (tb0 + (ok ? key : 0)) * 256 + kvh * 64 + 8 * ch;
;                 kv[i] = *(const v4u*)(CK + ro); vv[i] = *(const v4u*)(CV + ro); }
; #pragma unroll
;             for (int i = 0; i < 4; ++i) { const int c = tid + 512 * (4 * half + i), rw = c >> 3, ch = c & 7;
;                 *(LAS v4u*)(kimg + rw * 128 + ((ch ^ (rw & 7)) * 16)) = kv[i]; *(LAS v4u*)(vimg + rw * 128 + ch * 16) = vv[i]; }
.LBB0_1118:
	s_lshl_b32 s9, s39, 6
	s_ashr_i32 s8, s39, 7
	s_and_b32 s41, s9, 0x1f00
	s_ashr_i32 s9, s8, 31
	s_add_i32 s33, s41, s19
	s_lshl_b64 s[10:11], s[8:9], 13
	v_or_b32_e32 v4, s33, v139
	v_mov_b32_e32 v5, v3
	v_lshl_add_u64 v[6:7], s[10:11], 0, v[4:5]
	v_readlane_b32 s8, v255, 7
	s_and_b32 s40, s39, 3
	v_lshlrev_b64 v[8:9], 11, v[6:7]
	v_readlane_b32 s9, v255, 8
	s_lshl_b32 s16, s40, 9
	v_lshlrev_b32_e32 v2, 1, v138
	v_lshl_add_u64 v[8:9], s[8:9], 0, v[8:9]
	v_lshl_add_u64 v[8:9], v[8:9], 0, s[16:17]
	v_lshl_add_u64 v[144:145], v[8:9], 0, v[2:3]
	global_load_dwordx4 v[102:105], v[144:145], off
	global_load_dwordx4 v[106:109], v[144:145], off offset:32
	global_load_dwordx4 v[110:113], v[144:145], off offset:64
	global_load_dwordx4 v[114:117], v[144:145], off offset:96
	s_addk_i32 s41, 0xff80
	v_add_u32_e32 v2, s41, v157
	v_cmp_gt_u32_e32 vcc, s34, v2
	v_add_u32_e32 v5, s41, v158
	v_readlane_b32 s8, v255, 9
	v_cndmask_b32_e32 v8, 0, v2, vcc
	v_cmp_gt_u32_e32 vcc, s34, v5
	v_ashrrev_i32_e32 v9, 31, v8
	v_lshl_add_u64 v[8:9], s[10:11], 0, v[8:9]
	v_cndmask_b32_e32 v16, 0, v5, vcc
	v_add_u32_e32 v5, s41, v159
	v_cmp_gt_u32_e32 vcc, s34, v5
	v_ashrrev_i32_e32 v17, 31, v16
	v_lshlrev_b64 v[8:9], 9, v[8:9]
	v_cndmask_b32_e32 v24, 0, v5, vcc
	v_add_u32_e32 v5, s41, v160
	v_cmp_gt_u32_e32 vcc, s34, v5
	v_lshl_or_b32 v2, s40, 7, v182
	v_lshl_add_u64 v[16:17], s[10:11], 0, v[16:17]
	v_cndmask_b32_e32 v32, 0, v5, vcc
	v_add_u32_e32 v5, s41, v165
	v_cmp_gt_u32_e32 vcc, s34, v5
	v_ashrrev_i32_e32 v25, 31, v24
	v_or_b32_e32 v8, v8, v2
	v_cndmask_b32_e32 v40, 0, v5, vcc
	v_add_u32_e32 v5, s41, v166
	v_cmp_gt_u32_e32 vcc, s34, v5
	v_readlane_b32 s9, v255, 10
	v_lshlrev_b64 v[16:17], 9, v[16:17]
	v_cndmask_b32_e32 v48, 0, v5, vcc
	v_add_u32_e32 v5, s41, v167
	v_lshl_add_u64 v[24:25], s[10:11], 0, v[24:25]
	v_ashrrev_i32_e32 v33, 31, v32
	v_cmp_gt_u32_e32 vcc, s34, v5
	v_lshl_add_u64 v[10:11], s[8:9], 0, v[8:9]
	v_lshl_add_u64 v[12:13], s[12:13], 0, v[8:9]
	v_or_b32_e32 v16, v16, v2
	v_lshlrev_b64 v[24:25], 9, v[24:25]
	v_lshl_add_u64 v[32:33], s[10:11], 0, v[32:33]
	v_ashrrev_i32_e32 v41, 31, v40
	v_cndmask_b32_e32 v56, 0, v5, vcc
	v_add_u32_e32 v5, s41, v168
	global_load_dwordx4 v[8:11], v[10:11], off
	s_nop 0
	global_load_dwordx4 v[12:15], v[12:13], off
	v_lshl_add_u64 v[18:19], s[8:9], 0, v[16:17]
	v_lshl_add_u64 v[20:21], s[12:13], 0, v[16:17]
	v_or_b32_e32 v24, v24, v2
	v_lshlrev_b64 v[32:33], 9, v[32:33]
	v_lshl_add_u64 v[40:41], s[10:11], 0, v[40:41]
	v_ashrrev_i32_e32 v49, 31, v48
	v_cmp_gt_u32_e32 vcc, s34, v5
	global_load_dwordx4 v[16:19], v[18:19], off
	s_nop 0
	global_load_dwordx4 v[20:23], v[20:21], off
	v_lshl_add_u64 v[26:27], s[8:9], 0, v[24:25]
	v_lshl_add_u64 v[28:29], s[12:13], 0, v[24:25]
	v_or_b32_e32 v32, v32, v2
	v_lshlrev_b64 v[40:41], 9, v[40:41]
	v_lshl_add_u64 v[48:49], s[10:11], 0, v[48:49]
	v_ashrrev_i32_e32 v57, 31, v56
	v_cndmask_b32_e32 v64, 0, v5, vcc
	global_load_dwordx4 v[24:27], v[26:27], off
	s_nop 0
	global_load_dwordx4 v[28:31], v[28:29], off
	v_lshl_add_u64 v[34:35], s[8:9], 0, v[32:33]
	v_lshl_add_u64 v[36:37], s[12:13], 0, v[32:33]
	v_or_b32_e32 v40, v40, v2
	v_lshlrev_b64 v[48:49], 9, v[48:49]
	v_lshl_add_u64 v[56:57], s[10:11], 0, v[56:57]
	v_ashrrev_i32_e32 v65, 31, v64
	global_load_dwordx4 v[32:35], v[34:35], off
	s_nop 0
	global_load_dwordx4 v[36:39], v[36:37], off
	v_lshl_add_u64 v[42:43], s[8:9], 0, v[40:41]
	v_lshl_add_u64 v[44:45], s[12:13], 0, v[40:41]
	v_or_b32_e32 v48, v48, v2
	v_lshlrev_b64 v[56:57], 9, v[56:57]
	v_lshl_add_u64 v[64:65], s[10:11], 0, v[64:65]
	global_load_dwordx4 v[40:43], v[42:43], off
	s_nop 0
	global_load_dwordx4 v[44:47], v[44:45], off
	v_lshl_add_u64 v[50:51], s[8:9], 0, v[48:49]
	v_lshl_add_u64 v[52:53], s[12:13], 0, v[48:49]
	v_or_b32_e32 v56, v56, v2
	v_lshlrev_b64 v[68:69], 9, v[64:65]
	global_load_dwordx4 v[48:51], v[50:51], off
	s_nop 0
	global_load_dwordx4 v[52:55], v[52:53], off
	v_lshl_add_u64 v[58:59], s[8:9], 0, v[56:57]
	v_lshl_add_u64 v[60:61], s[12:13], 0, v[56:57]
	v_or_b32_e32 v68, v68, v2
	global_load_dwordx4 v[56:59], v[58:59], off
	s_nop 0
	global_load_dwordx4 v[60:63], v[60:61], off
	v_lshl_add_u64 v[64:65], s[8:9], 0, v[68:69]
	v_lshl_add_u64 v[68:69], s[12:13], 0, v[68:69]
	global_load_dwordx4 v[64:67], v[64:65], off
	v_add_u32_e32 v2, v143, v161
	global_load_dwordx4 v[68:71], v[68:69], off
	s_waitcnt lgkmcnt(0)
	s_barrier
	s_and_saveexec_b64 s[22:23], s[2:3]
	v_mov_b32_e32 v73, 0
	s_cbranch_execz .LBB0_1131
	s_lshl_b32 s16, s40, 7
	s_mov_b64 s[24:25], 0
	v_mov_b32_e32 v74, v173
	v_mov_b32_e32 v75, v1
	s_branch .LBB0_1121
.LBB0_1120:
	s_or_b64 exec, exec, s[8:9]
	v_add_u32_e32 v72, 0x200, v75
	v_cmp_lt_i32_e32 vcc, s31, v75
	ds_write2st64_b32 v74, v76, v77 offset0:12 offset1:18
	v_add_u32_e32 v74, 0x800, v74
	s_or_b64 s[24:25], vcc, s[24:25]
	v_mov_b32_e32 v75, v72
	s_andn2_b64 exec, exec, s[24:25]
	s_cbranch_execz .LBB0_1131
; #define LAS __attribute__((address_space(3)))
; __device__ __forceinline__ void mixer_c_shared(const bf16* CQ, const bf16* CK, const bf16* CV  , bf16* O, const float* rel_bias, const float* sink, LAS unsigned char* lds, int G, int blk, int tid, int lane, int wave) {
;     ...
;         for (int idx = tid; idx < TC_LEN; idx += NWAVES * 64) { const int i = idx - TC_OFF; const bool in = (i >= 0 && i <= 256); const int bk = in ? t5_bucket(i - 128) : 0;
; #pragma unroll
;             for (int j = 0; j < 4; ++j) tab4[j * TC_LEN + idx] = in ? (rel_bias[(4 * kvh + j) * 32 + bk] * LOG2E + 64.0f) * KAPPA : -1.0f; }
; #pragma unroll
;         for (int half = 0; half < 2; ++half) {
;             v4u kv[4], vv[4];
; #pragma unroll
;             for (int i = 0; i < 4; ++i) { const int c = tid + 512 * (4 * half + i), rw = c >> 3, ch = c & 7, key = w0 + rw; const bool ok = key >= 0 && key < SEQ; const size_t ro = (tb0 + (ok ? key : 0)) * 256 + kvh * 64 + 8 * ch;
;                 kv[i] = *(const v4u*)(CK + ro); vv[i] = *(const v4u*)(CV + ro); }
; #pragma unroll
;             for (int i = 0; i < 4; ++i) { const int c = tid + 512 * (4 * half + i), rw = c >> 3, ch = c & 7;
;                 *(LAS v4u*)(kimg + rw * 128 + ((ch ^ (rw & 7)) * 16)) = kv[i]; *(LAS v4u*)(vimg + rw * 128 + ch * 16) = vv[i]; }
;         }
;         __syncthreads();
.LBB0_1121:
	v_subrev_u32_e32 v72, 32, v75
	s_movk_i32 s8, 0x100
	v_cmp_lt_u32_e32 vcc, s8, v72
	s_movk_i32 s8, 0x101
	v_cmp_gt_u32_e64 s[8:9], s8, v72
	v_mov_b32_e32 v72, 0
	s_and_saveexec_b64 s[26:27], s[8:9]
	s_cbranch_execz .LBB0_1127
	v_add_u32_e32 v72, 0xffffff60, v75
	v_sub_u32_e32 v76, 0xa0, v75
	v_max_i32_e32 v77, v72, v76
	v_cmp_lt_u32_e64 s[8:9], s21, v75
	s_nop 1
	v_cndmask_b32_e64 v76, 0, 16, s[8:9]
	v_cmp_lt_u32_e64 s[8:9], 7, v77
	s_and_saveexec_b64 s[28:29], s[8:9]
	s_xor_b64 s[28:29], exec, s[28:29]
	s_cbranch_execz .LBB0_1124
	v_cmp_lt_u32_e64 s[8:9], 14, v77
	s_nop 1
	v_cndmask_b32_e64 v72, 8, 9, s[8:9]
	v_cmp_lt_u32_e64 s[8:9], 26, v77
	s_nop 1
	v_cndmask_b32_e64 v78, 0, 1, s[8:9]
	v_cmp_lt_u32_e64 s[8:9], 49, v77
	v_or_b32_e32 v76, v76, v78
	v_add_u32_e32 v72, v76, v72
	v_cndmask_b32_e64 v80, 0, 1, s[8:9]
	v_cmp_lt_u32_e64 s[8:9], s30, v77
	s_nop 1
	v_addc_co_u32_e64 v72, s[8:9], v72, v80, s[8:9]
.LBB0_1124:
	s_andn2_saveexec_b64 s[8:9], s[28:29]
	v_or_b32_e32 v72, v76, v77
	s_or_b64 exec, exec, s[8:9]
.LBB0_1127:
	s_or_b64 exec, exec, s[26:27]
	s_and_saveexec_b64 s[8:9], vcc
	s_xor_b64 s[8:9], exec, s[8:9]
	ds_write2st64_b32 v74, v181, v181 offset1:6
	s_or_saveexec_b64 s[8:9], s[8:9]
	v_mov_b32_e32 v76, -1.0
	v_mov_b32_e32 v77, -1.0
	s_xor_b64 exec, exec, s[8:9]
	s_cbranch_execz .LBB0_1120
	v_readlane_b32 s44, v254, 14
	v_add_u32_e32 v72, s16, v72
	v_readlane_b32 s46, v254, 16
	v_readlane_b32 s47, v254, 17
	v_readlane_b32 s45, v254, 15
	v_readlane_b32 s48, v254, 18
	v_lshl_add_u64 v[76:77], v[72:73], 2, s[46:47]
	global_load_dword v72, v[76:77], off
	global_load_dword v78, v[76:77], off offset:128
	global_load_dword v80, v[76:77], off offset:256
	global_load_dword v81, v[76:77], off offset:384
	v_readlane_b32 s49, v254, 19
	v_readlane_b32 s50, v254, 20
	v_readlane_b32 s51, v254, 21
	v_readlane_b32 s52, v254, 22
	v_readlane_b32 s53, v254, 23
	v_readlane_b32 s54, v254, 24
	v_readlane_b32 s55, v254, 25
	v_readlane_b32 s56, v254, 26
	v_readlane_b32 s57, v254, 27
	v_readlane_b32 s58, v254, 28
	v_readlane_b32 s59, v254, 29
	s_waitcnt vmcnt(3)
	v_fmamk_f32 v72, v72, 0x3fb8aa3b, v142
	s_waitcnt vmcnt(2)
	v_fmamk_f32 v78, v78, 0x3fb8aa3b, v142
	v_mul_f32_e32 v72, 0x3b000080, v72
	s_waitcnt vmcnt(0)
	v_pk_fma_f32 v[76:77], v[80:81], s[18:19], v[142:143] op_sel_hi:[1,0,0]
	v_mul_f32_e32 v78, 0x3b000080, v78
	v_pk_mul_f32 v[76:77], v[76:77], s[20:21] op_sel_hi:[1,0]
	ds_write2st64_b32 v74, v72, v78 offset1:6
	s_branch .LBB0_1120
.LBB0_1131:
	s_or_b64 exec, exec, s[22:23]
	s_sub_i32 s8, 0x80, s33
	s_lshl_b32 s24, s40, 2
	s_lshr_b32 s11, s8, 5
	v_lshlrev_b64 v[6:7], 10, v[6:7]
	s_waitcnt vmcnt(16)
	v_mov_b64_e32 v[86:87], v[102:103]
	v_mov_b64_e32 v[90:91], v[106:107]
	v_mov_b64_e32 v[94:95], v[110:111]
	v_mov_b64_e32 v[98:99], v[114:115]
	s_mov_b32 s25, 0
	v_sub_u32_e32 v194, v138, v4
	v_lshl_add_u64 v[146:147], v[140:141], 0, v[6:7]
	v_mov_b64_e32 v[88:89], v[104:105]
	v_mov_b64_e32 v[92:93], v[108:109]
	v_mov_b64_e32 v[96:97], v[112:113]
	v_mov_b64_e32 v[100:101], v[116:117]
	s_waitcnt vmcnt(15)
	ds_write_b128 v183, v[8:11] offset:6144
	s_waitcnt vmcnt(14)
	ds_write_b128 v2, v[12:15]
	s_waitcnt vmcnt(13)
	ds_write_b128 v184, v[16:19] offset:6144
	v_add_u32_e32 v2, v143, v162
	s_waitcnt vmcnt(12)
	ds_write_b128 v2, v[20:23]
	s_waitcnt vmcnt(11)
	ds_write_b128 v185, v[24:27] offset:6144
	v_add_u32_e32 v2, v143, v163
	s_waitcnt vmcnt(10)
	ds_write_b128 v2, v[28:31]
	s_waitcnt vmcnt(9)
	ds_write_b128 v186, v[32:35] offset:6144
	v_add_u32_e32 v2, v143, v164
	s_waitcnt vmcnt(8)
	ds_write_b128 v2, v[36:39]
	s_waitcnt vmcnt(7)
	ds_write_b128 v187, v[40:43] offset:6144
	v_add_u32_e32 v2, v143, v169
	s_waitcnt vmcnt(6)
	ds_write_b128 v2, v[44:47]
	s_waitcnt vmcnt(5)
	ds_write_b128 v188, v[48:51] offset:6144
	v_add_u32_e32 v2, v143, v170
	s_waitcnt vmcnt(4)
	ds_write_b128 v2, v[52:55]
	s_waitcnt vmcnt(3)
	ds_write_b128 v189, v[56:59] offset:6144
	v_add_u32_e32 v2, v143, v171
	s_waitcnt vmcnt(2)
	ds_write_b128 v2, v[60:63]
	s_waitcnt vmcnt(1)
	ds_write_b128 v190, v[64:67] offset:6144
	v_add_u32_e32 v2, v143, v172
	s_waitcnt vmcnt(0)
	ds_write_b128 v2, v[68:71]
	v_sub_co_u32_e32 v2, vcc, s33, v191
	s_and_b64 s[8:9], vcc, exec
	s_cselect_b32 s26, s11, 0
	s_sub_i32 s8, 0x2080, s33
	s_ashr_i32 s8, s8, 5
	s_min_i32 s27, s8, 9
	s_add_i32 s8, s26, 1
	s_cmp_lt_i32 s8, s27
	v_readfirstlane_b32 s10, v2
	s_cselect_b64 s[22:23], -1, 0
	s_lshl_b32 s8, s26, 7
	s_lshl_b32 s28, s26, 12
	v_add_u32_e32 v195, s8, v175
	v_add_u32_e32 v196, s8, v174
	v_add_u32_e32 v197, s28, v176
	v_add_u32_e32 v198, s28, v177
	v_add_u32_e32 v199, s28, v178
	v_add_u32_e32 v200, s28, v179
	v_add_u32_e32 v201, s28, v180
	s_lshl_b32 s29, s10, 2
	s_waitcnt lgkmcnt(0)
	s_barrier
